# MoBA attention steady loops: 4 of the 8 QK MFMAs per tile moved back into the softmax VALU groups (hipcc had bunched all 8 behind them)
# baseline (speedup 1.0000x reference)
.LBB0_996:
	s_add_i32 s22, s21, -5
	v_add_u32_e32 v3, s0, v233
	ds_read_b64_tr_b16 v[190:191], v3 offset:24576
	ds_read_b64_tr_b16 v[192:193], v3 offset:25088
	v_add_f32_e32 v4, v82, v83
	v_add_f32_e32 v4, v84, v4
	v_add_f32_e32 v4, v85, v4
	v_add_f32_e32 v4, v86, v4
	v_add_f32_e32 v4, v87, v4
	v_cvt_pk_bf16_f32 v114, v82, v83
	v_cvt_pk_bf16_f32 v115, v84, v85
	ds_read_b64_tr_b16 v[186:187], v3 offset:28672
	ds_read_b64_tr_b16 v[188:189], v3 offset:29184
	v_add_f32_e32 v4, v88, v4
	v_add_f32_e32 v4, v89, v4
	v_add_f32_e32 v4, v90, v4
	v_add_f32_e32 v4, v91, v4
	v_cvt_pk_bf16_f32 v116, v86, v87
	v_cvt_pk_bf16_f32 v117, v88, v89
	ds_read_b64_tr_b16 v[182:183], v3 offset:25600
	ds_read_b64_tr_b16 v[184:185], v3 offset:26112
	v_add_f32_e32 v4, v92, v4
	v_add_f32_e32 v4, v93, v4
	v_add_f32_e32 v4, v94, v4
	v_add_f32_e32 v4, v95, v4
	v_cvt_pk_bf16_f32 v118, v90, v91
	v_cvt_pk_bf16_f32 v119, v92, v93
	ds_read_b64_tr_b16 v[178:179], v3 offset:29696
	ds_read_b64_tr_b16 v[180:181], v3 offset:30208
	v_add_f32_e32 v4, v96, v4
	v_add_f32_e32 v4, v97, v4
	v_add_f32_e32 v4, v66, v4
	v_add_f32_e32 v4, v67, v4
	v_cvt_pk_bf16_f32 v120, v94, v95
	v_cvt_pk_bf16_f32 v121, v96, v97
	ds_read_b64_tr_b16 v[174:175], v3 offset:26624
	ds_read_b64_tr_b16 v[176:177], v3 offset:27136
	s_waitcnt lgkmcnt(10)
	v_mfma_f32_32x32x16_bf16 v[82:97], v[130:133], v[110:113], v[50:65]
	v_add_f32_e32 v4, v68, v4
	v_add_f32_e32 v4, v69, v4
	v_add_f32_e32 v4, v70, v4
	v_add_f32_e32 v4, v71, v4
	v_cvt_pk_bf16_f32 v122, v66, v67
	v_cvt_pk_bf16_f32 v123, v68, v69
	ds_read_b64_tr_b16 v[170:171], v3 offset:30720
	ds_read_b64_tr_b16 v[172:173], v3 offset:31232
	v_mfma_f32_32x32x16_bf16 v[82:97], v[142:145], v[106:109], v[82:97]
	v_add_f32_e32 v4, v72, v4
	v_add_f32_e32 v4, v73, v4
	v_add_f32_e32 v4, v74, v4
	v_add_f32_e32 v4, v75, v4
	v_cvt_pk_bf16_f32 v124, v70, v71
	v_cvt_pk_bf16_f32 v125, v72, v73
	ds_read_b64_tr_b16 v[166:167], v3 offset:27648
	ds_read_b64_tr_b16 v[168:169], v3 offset:28160
	v_mfma_f32_32x32x16_bf16 v[82:97], v[150:153], v[102:105], v[82:97]
	v_add_f32_e32 v4, v76, v4
	v_add_f32_e32 v4, v77, v4
	v_add_f32_e32 v4, v78, v4
	v_add_f32_e32 v4, v79, v4
	v_cvt_pk_bf16_f32 v126, v74, v75
	v_cvt_pk_bf16_f32 v127, v76, v77
	ds_read_b64_tr_b16 v[162:163], v3 offset:31744
	ds_read_b64_tr_b16 v[164:165], v3 offset:32256
	v_mfma_f32_32x32x16_bf16 v[82:97], v[158:161], v[98:101], v[82:97]
	v_add_f32_e32 v3, v80, v4
	v_add_f32_e32 v3, v81, v3
	v_add_f32_e32 v3, 0, v3
	v_cvt_pk_bf16_f32 v128, v78, v79
	v_cvt_pk_bf16_f32 v129, v80, v81
	s_waitcnt lgkmcnt(14)
	v_lshl_add_u64 v[4:5], v[200:201], 0, s[68:69]
	s_add_i32 s0, s54, s62
	s_mov_b32 s1, m0
	s_mov_b32 m0, s0
	s_nop 0
	global_load_lds_dwordx4 v[4:5], off
	s_mov_b32 m0, s1
	v_lshl_add_u64 v[4:5], v[198:199], 0, s[68:69]
	s_add_i32 s0, s20, s63
	s_mov_b32 s1, m0
	s_mov_b32 m0, s0
	s_nop 0
	global_load_lds_dwordx4 v[4:5], off
	s_mov_b32 m0, s1
	s_cmp_lt_i32 s22, s61
	v_mfma_f32_32x32x16_bf16 v[66:81], v[134:137], v[110:113], v[50:65]
	v_mfma_f32_32x32x16_bf16 v[66:81], v[138:141], v[106:109], v[66:81]
	v_mfma_f32_32x32x16_bf16 v[66:81], v[146:149], v[102:105], v[66:81]
	v_mfma_f32_32x32x16_bf16 v[66:81], v[154:157], v[98:101], v[66:81]
	s_cbranch_scc1 .LBB0_998
	ds_read_b128 v[4:7], v235
	ds_read_b128 v[8:11], v235 offset:128
	ds_read_b128 v[12:15], v235 offset:32
	ds_read_b128 v[130:133], v235 offset:160
	s_waitcnt lgkmcnt(3)
	v_sub_u32_e32 v4, v224, v4
	v_sub_u32_e32 v5, v224, v5
	v_sub_u32_e32 v6, v224, v6
	v_sub_u32_e32 v7, v224, v7
	s_waitcnt lgkmcnt(2)
	v_sub_u32_e32 v8, v224, v8
	v_med3_i32 v4, v4, 0, v222
	v_med3_i32 v5, v5, 0, v222
	v_sub_u32_e32 v9, v224, v9
	v_med3_i32 v6, v6, 0, v222
	v_sub_u32_e32 v10, v224, v10
	v_med3_i32 v7, v7, 0, v222
	v_sub_u32_e32 v11, v224, v11
	v_med3_i32 v8, v8, 0, v222
	v_lshl_add_u32 v4, v4, 2, s55
	v_med3_i32 v9, v9, 0, v222
	v_lshl_add_u32 v5, v5, 2, s55
	v_med3_i32 v10, v10, 0, v222
	v_lshl_add_u32 v6, v6, 2, s55
	v_med3_i32 v11, v11, 0, v222
	v_lshl_add_u32 v7, v7, 2, s55
	v_lshl_add_u32 v8, v8, 2, s55
	v_lshl_add_u32 v9, v9, 2, s55
	v_lshl_add_u32 v10, v10, 2, s55
	v_lshl_add_u32 v11, v11, 2, s55
	ds_read_b32 v134, v4
	ds_read_b32 v4, v8
	ds_read_b32 v135, v5
	ds_read_b32 v5, v9
	ds_read_b32 v136, v6
	ds_read_b32 v138, v10
	ds_read_b32 v137, v7
	ds_read_b32 v139, v11
	s_waitcnt lgkmcnt(9)
	v_sub_u32_e32 v6, v224, v12
	s_waitcnt lgkmcnt(8)
	v_sub_u32_e32 v7, v224, v130
	v_med3_i32 v6, v6, 0, v222
	v_med3_i32 v7, v7, 0, v222
	v_lshl_add_u32 v10, v6, 2, s55
	v_lshl_add_u32 v11, v7, 2, s55
	v_sub_u32_e32 v6, v224, v13
	v_sub_u32_e32 v7, v224, v131
	v_med3_i32 v6, v6, 0, v222
	v_med3_i32 v7, v7, 0, v222
	v_lshl_add_u32 v12, v6, 2, s55
	v_lshl_add_u32 v13, v7, 2, s55
	v_sub_u32_e32 v6, v224, v14
	v_sub_u32_e32 v7, v224, v132
	v_med3_i32 v6, v6, 0, v222
	v_med3_i32 v7, v7, 0, v222
	v_lshl_add_u32 v14, v6, 2, s55
	v_lshl_add_u32 v16, v7, 2, s55
	v_sub_u32_e32 v6, v224, v15
	v_sub_u32_e32 v7, v224, v133
	v_med3_i32 v6, v6, 0, v222
	v_med3_i32 v7, v7, 0, v222
	v_lshl_add_u32 v15, v6, 2, s55
	v_lshl_add_u32 v17, v7, 2, s55
	ds_read_b128 v[6:9], v235 offset:64
	ds_read_b32 v140, v10
	ds_read_b32 v142, v11
	ds_read_b32 v141, v12
	ds_read_b32 v143, v13
	ds_read_b32 v144, v14
	ds_read_b32 v146, v16
	ds_read_b32 v145, v15
	ds_read_b32 v147, v17
	ds_read_b128 v[10:13], v235 offset:192
	ds_read_b128 v[14:17], v235 offset:96
	ds_read_b128 v[130:133], v235 offset:224
	s_waitcnt lgkmcnt(11)
	v_sub_u32_e32 v8, v224, v8
	v_med3_i32 v8, v8, 0, v222
	v_sub_u32_e32 v6, v224, v6
	s_waitcnt lgkmcnt(2)
	v_sub_u32_e32 v10, v224, v10
	v_sub_u32_e32 v7, v224, v7
	v_sub_u32_e32 v11, v224, v11
	v_sub_u32_e32 v12, v224, v12
	v_lshl_add_u32 v148, v8, 2, s55
	v_sub_u32_e32 v8, v224, v9
	v_med3_i32 v6, v6, 0, v222
	v_med3_i32 v10, v10, 0, v222
	v_med3_i32 v7, v7, 0, v222
	v_med3_i32 v11, v11, 0, v222
	v_med3_i32 v12, v12, 0, v222
	v_med3_i32 v8, v8, 0, v222
	v_sub_u32_e32 v9, v224, v13
	s_waitcnt lgkmcnt(0)
	v_sub_u32_e32 v131, v224, v131
	v_sub_u32_e32 v16, v224, v16
	v_lshl_add_u32 v6, v6, 2, s55
	v_lshl_add_u32 v10, v10, 2, s55
	v_lshl_add_u32 v7, v7, 2, s55
	v_lshl_add_u32 v11, v11, 2, s55
	v_lshl_add_u32 v12, v12, 2, s55
	v_med3_i32 v9, v9, 0, v222
	v_lshl_add_u32 v13, v8, 2, s55
	v_med3_i32 v131, v131, 0, v222
	v_med3_i32 v16, v16, 0, v222
	v_lshl_add_u32 v149, v9, 2, s55
	ds_read_b32 v6, v6
	ds_read_b32 v8, v10
	ds_read_b32 v7, v7
	ds_read_b32 v9, v11
	ds_read_b32 v10, v148
	ds_read_b32 v12, v12
	ds_read_b32 v11, v13
	ds_read_b32 v13, v149
	v_sub_u32_e32 v14, v224, v14
	v_sub_u32_e32 v130, v224, v130
	v_sub_u32_e32 v15, v224, v15
	v_lshl_add_u32 v148, v131, 2, s55
	v_sub_u32_e32 v131, v224, v132
	v_lshl_add_u32 v132, v16, 2, s55
	v_sub_u32_e32 v16, v224, v17
	v_sub_u32_e32 v17, v224, v133
	v_med3_i32 v14, v14, 0, v222
	v_med3_i32 v130, v130, 0, v222
	v_med3_i32 v15, v15, 0, v222
	v_med3_i32 v131, v131, 0, v222
	v_med3_i32 v16, v16, 0, v222
	v_med3_i32 v17, v17, 0, v222
	v_lshl_add_u32 v14, v14, 2, s55
	v_lshl_add_u32 v130, v130, 2, s55
	v_lshl_add_u32 v15, v15, 2, s55
	v_lshl_add_u32 v149, v131, 2, s55
	v_lshl_add_u32 v131, v16, 2, s55
	v_lshl_add_u32 v17, v17, 2, s55
	ds_read_b32 v14, v14
	ds_read_b32 v16, v130
	ds_read_b32 v130, v132
	ds_read_b32 v131, v131
	ds_read_b32 v15, v15
	ds_read_b32 v133, v17
	ds_read_b32 v132, v149
	ds_read_b32 v17, v148
	s_waitcnt lgkmcnt(4)
	v_pk_add_f32 v[96:97], v[96:97], v[130:131]
	s_waitcnt lgkmcnt(3)
	v_pk_add_f32 v[94:95], v[94:95], v[14:15]
	v_pk_add_f32 v[92:93], v[92:93], v[10:11]
	v_pk_add_f32 v[90:91], v[90:91], v[6:7]
	v_pk_add_f32 v[88:89], v[88:89], v[144:145]
	v_pk_add_f32 v[86:87], v[86:87], v[140:141]
	v_pk_add_f32 v[84:85], v[84:85], v[136:137]
	v_pk_add_f32 v[82:83], v[82:83], v[134:135]
	s_waitcnt lgkmcnt(1)
	v_pk_add_f32 v[80:81], v[80:81], v[132:133]
	s_waitcnt lgkmcnt(0)
	v_pk_add_f32 v[78:79], v[78:79], v[16:17]
	v_pk_add_f32 v[76:77], v[76:77], v[12:13]
	v_pk_add_f32 v[74:75], v[74:75], v[8:9]
	v_pk_add_f32 v[72:73], v[72:73], v[146:147]
	v_pk_add_f32 v[70:71], v[70:71], v[142:143]
	v_pk_add_f32 v[68:69], v[68:69], v[138:139]
	v_pk_add_f32 v[66:67], v[66:67], v[4:5]

.LBB0_1001:
	s_add_i32 s0, s21, -4
	s_add_i32 s1, s20, 0x2000
	v_add_u32_e32 v16, s54, v233
	ds_read_b64_tr_b16 v[134:135], v16 offset:24576
	ds_read_b64_tr_b16 v[136:137], v16 offset:25088
	v_add_f32_e32 v4, v82, v83
	v_add_f32_e32 v4, v84, v4
	v_add_f32_e32 v4, v85, v4
	v_add_f32_e32 v4, v86, v4
	v_add_f32_e32 v4, v87, v4
	v_cvt_pk_bf16_f32 v114, v82, v83
	v_cvt_pk_bf16_f32 v115, v84, v85
	ds_read_b64_tr_b16 v[130:131], v16 offset:28672
	ds_read_b64_tr_b16 v[132:133], v16 offset:29184
	v_add_f32_e32 v4, v88, v4
	v_add_f32_e32 v4, v89, v4
	v_add_f32_e32 v4, v90, v4
	v_add_f32_e32 v4, v91, v4
	v_cvt_pk_bf16_f32 v116, v86, v87
	v_cvt_pk_bf16_f32 v117, v88, v89
	ds_read_b64_tr_b16 v[138:139], v16 offset:25600
	ds_read_b64_tr_b16 v[140:141], v16 offset:26112
	v_add_f32_e32 v4, v92, v4
	v_add_f32_e32 v4, v93, v4
	v_add_f32_e32 v4, v94, v4
	v_add_f32_e32 v4, v95, v4
	v_cvt_pk_bf16_f32 v12, v90, v91
	v_cvt_pk_bf16_f32 v13, v92, v93
	ds_read_b64_tr_b16 v[146:147], v16 offset:29696
	ds_read_b64_tr_b16 v[148:149], v16 offset:30208
	v_add_f32_e32 v4, v96, v4
	v_add_f32_e32 v4, v97, v4
	v_add_f32_e32 v4, v66, v4
	v_add_f32_e32 v4, v67, v4
	v_cvt_pk_bf16_f32 v14, v94, v95
	v_cvt_pk_bf16_f32 v15, v96, v97
	ds_read_b64_tr_b16 v[154:155], v16 offset:26624
	ds_read_b64_tr_b16 v[156:157], v16 offset:27136
	s_waitcnt lgkmcnt(10)
	v_mfma_f32_32x32x16_bf16 v[82:97], v[118:121], v[110:113], v[50:65]
	v_add_f32_e32 v4, v68, v4
	v_add_f32_e32 v4, v69, v4
	v_add_f32_e32 v4, v70, v4
	v_add_f32_e32 v4, v71, v4
	v_cvt_pk_bf16_f32 v8, v66, v67
	v_cvt_pk_bf16_f32 v9, v68, v69
	ds_read_b64_tr_b16 v[170:171], v16 offset:30720
	ds_read_b64_tr_b16 v[172:173], v16 offset:31232
	v_mfma_f32_32x32x16_bf16 v[82:97], v[142:145], v[106:109], v[82:97]
	v_add_f32_e32 v4, v72, v4
	v_add_f32_e32 v4, v73, v4
	v_add_f32_e32 v4, v74, v4
	v_add_f32_e32 v4, v75, v4
	v_cvt_pk_bf16_f32 v10, v70, v71
	v_cvt_pk_bf16_f32 v11, v72, v73
	ds_read_b64_tr_b16 v[166:167], v16 offset:27648
	ds_read_b64_tr_b16 v[168:169], v16 offset:28160
	v_mfma_f32_32x32x16_bf16 v[82:97], v[158:161], v[102:105], v[82:97]
	v_add_f32_e32 v4, v76, v4
	v_add_f32_e32 v4, v77, v4
	v_add_f32_e32 v4, v78, v4
	v_add_f32_e32 v17, v79, v4
	v_cvt_pk_bf16_f32 v4, v74, v75
	v_cvt_pk_bf16_f32 v5, v76, v77
	ds_read_b64_tr_b16 v[162:163], v16 offset:31744
	ds_read_b64_tr_b16 v[164:165], v16 offset:32256
	v_mfma_f32_32x32x16_bf16 v[82:97], v[178:181], v[98:101], v[82:97]
	v_add_f32_e32 v6, v80, v17
	v_add_f32_e32 v6, v81, v6
	v_add_f32_e32 v182, 0, v6
	v_cvt_pk_bf16_f32 v6, v78, v79
	v_cvt_pk_bf16_f32 v7, v80, v81
	s_waitcnt lgkmcnt(14)
	s_cmpk_lg_i32 s20, 0x4000
	s_cselect_b32 s54, s1, 0
	s_add_i32 s1, s20, s62
	s_mov_b32 s8, m0
	s_mov_b32 m0, s1
	s_nop 0
	global_load_lds_dwordx4 v[200:201], off
	s_mov_b32 m0, s8
	s_add_i32 s1, s54, s63
	s_mov_b32 s8, m0
	s_mov_b32 m0, s1
	s_nop 0
	global_load_lds_dwordx4 v[198:199], off
	s_mov_b32 m0, s8
	s_cmp_lt_i32 s0, s61
	v_mfma_f32_32x32x16_bf16 v[66:81], v[122:125], v[110:113], v[50:65]
	v_mfma_f32_32x32x16_bf16 v[66:81], v[126:129], v[106:109], v[66:81]
	v_mfma_f32_32x32x16_bf16 v[66:81], v[150:153], v[102:105], v[66:81]
	v_mfma_f32_32x32x16_bf16 v[66:81], v[174:177], v[98:101], v[66:81]
	s_cbranch_scc1 .LBB0_1003
	ds_read_b128 v[118:121], v235 offset:256
	ds_read_b128 v[122:125], v235 offset:384
	ds_read_b128 v[126:129], v235 offset:288
	ds_read_b128 v[142:145], v235 offset:416
	s_waitcnt lgkmcnt(3)
	v_sub_u32_e32 v16, v224, v118
	s_waitcnt lgkmcnt(2)
	v_sub_u32_e32 v17, v224, v122
	v_sub_u32_e32 v118, v224, v119
	v_sub_u32_e32 v119, v224, v123
	v_med3_i32 v16, v16, 0, v222
	v_med3_i32 v17, v17, 0, v222
	v_med3_i32 v118, v118, 0, v222
	v_med3_i32 v119, v119, 0, v222
	v_sub_u32_e32 v120, v224, v120
	v_sub_u32_e32 v122, v224, v124
	v_sub_u32_e32 v121, v224, v121
	v_sub_u32_e32 v123, v224, v125
	v_lshl_add_u32 v16, v16, 2, s55
	v_lshl_add_u32 v17, v17, 2, s55
	v_lshl_add_u32 v118, v118, 2, s55
	v_lshl_add_u32 v119, v119, 2, s55
	v_med3_i32 v120, v120, 0, v222
	v_med3_i32 v122, v122, 0, v222
	v_med3_i32 v121, v121, 0, v222
	v_med3_i32 v123, v123, 0, v222
	v_lshl_add_u32 v120, v120, 2, s55
	v_lshl_add_u32 v122, v122, 2, s55
	v_lshl_add_u32 v121, v121, 2, s55
	v_lshl_add_u32 v123, v123, 2, s55
	ds_read_b32 v150, v16
	ds_read_b32 v16, v17
	ds_read_b32 v151, v118
	ds_read_b32 v17, v119
	ds_read_b32 v152, v120
	ds_read_b32 v158, v122
	ds_read_b32 v153, v121
	ds_read_b32 v159, v123
	s_waitcnt lgkmcnt(9)
	v_sub_u32_e32 v118, v224, v126
	s_waitcnt lgkmcnt(8)
	v_sub_u32_e32 v119, v224, v142
	v_med3_i32 v118, v118, 0, v222
	v_med3_i32 v119, v119, 0, v222
	v_lshl_add_u32 v122, v118, 2, s55
	v_lshl_add_u32 v123, v119, 2, s55
	v_sub_u32_e32 v118, v224, v127
	v_sub_u32_e32 v119, v224, v143
	v_med3_i32 v118, v118, 0, v222
	v_med3_i32 v119, v119, 0, v222
	v_lshl_add_u32 v124, v118, 2, s55
	v_lshl_add_u32 v125, v119, 2, s55
	v_sub_u32_e32 v118, v224, v128
	v_sub_u32_e32 v119, v224, v144
	v_med3_i32 v118, v118, 0, v222
	v_med3_i32 v119, v119, 0, v222
	v_lshl_add_u32 v126, v118, 2, s55
	v_lshl_add_u32 v127, v119, 2, s55
	v_sub_u32_e32 v118, v224, v129
	v_sub_u32_e32 v119, v224, v145
	v_med3_i32 v118, v118, 0, v222
	v_med3_i32 v119, v119, 0, v222
	v_lshl_add_u32 v128, v118, 2, s55
	v_lshl_add_u32 v129, v119, 2, s55
	ds_read_b128 v[118:121], v235 offset:320
	ds_read_b32 v160, v122
	ds_read_b32 v174, v123
	ds_read_b32 v161, v124
	ds_read_b32 v175, v125
	ds_read_b32 v176, v126
	ds_read_b32 v178, v127
	ds_read_b32 v177, v128
	ds_read_b32 v179, v129
	ds_read_b128 v[122:125], v235 offset:448
	ds_read_b128 v[126:129], v235 offset:352
	ds_read_b128 v[142:145], v235 offset:480
	s_waitcnt lgkmcnt(11)
	v_sub_u32_e32 v120, v224, v120
	v_med3_i32 v120, v120, 0, v222
	v_sub_u32_e32 v118, v224, v118
	s_waitcnt lgkmcnt(2)
	v_sub_u32_e32 v122, v224, v122
	v_sub_u32_e32 v119, v224, v119
	v_sub_u32_e32 v123, v224, v123
	v_sub_u32_e32 v124, v224, v124
	v_lshl_add_u32 v180, v120, 2, s55
	v_sub_u32_e32 v120, v224, v121
	v_med3_i32 v118, v118, 0, v222
	v_med3_i32 v122, v122, 0, v222
	v_med3_i32 v119, v119, 0, v222
	v_med3_i32 v123, v123, 0, v222
	v_med3_i32 v124, v124, 0, v222
	v_med3_i32 v120, v120, 0, v222
	v_sub_u32_e32 v121, v224, v125
	s_waitcnt lgkmcnt(0)
	v_sub_u32_e32 v143, v224, v143
	v_sub_u32_e32 v128, v224, v128
	v_lshl_add_u32 v118, v118, 2, s55
	v_lshl_add_u32 v122, v122, 2, s55
	v_lshl_add_u32 v119, v119, 2, s55
	v_lshl_add_u32 v123, v123, 2, s55
	v_lshl_add_u32 v124, v124, 2, s55
	v_med3_i32 v121, v121, 0, v222
	v_lshl_add_u32 v125, v120, 2, s55
	v_med3_i32 v143, v143, 0, v222
	v_med3_i32 v128, v128, 0, v222
	v_lshl_add_u32 v181, v121, 2, s55
	ds_read_b32 v118, v118
	ds_read_b32 v120, v122
	ds_read_b32 v119, v119
	ds_read_b32 v121, v123
	ds_read_b32 v122, v180
	ds_read_b32 v124, v124
	ds_read_b32 v123, v125
	ds_read_b32 v125, v181
	v_sub_u32_e32 v126, v224, v126
	v_sub_u32_e32 v142, v224, v142
	v_sub_u32_e32 v127, v224, v127
	v_lshl_add_u32 v180, v143, 2, s55
	v_sub_u32_e32 v143, v224, v144
	v_lshl_add_u32 v144, v128, 2, s55
	v_sub_u32_e32 v128, v224, v129
	v_sub_u32_e32 v129, v224, v145
	v_med3_i32 v126, v126, 0, v222
	v_med3_i32 v142, v142, 0, v222
	v_med3_i32 v127, v127, 0, v222
	v_med3_i32 v143, v143, 0, v222
	v_med3_i32 v128, v128, 0, v222
	v_med3_i32 v129, v129, 0, v222
	v_lshl_add_u32 v126, v126, 2, s55
	v_lshl_add_u32 v142, v142, 2, s55
	v_lshl_add_u32 v127, v127, 2, s55
	v_lshl_add_u32 v181, v143, 2, s55
	v_lshl_add_u32 v143, v128, 2, s55
	v_lshl_add_u32 v129, v129, 2, s55
	ds_read_b32 v126, v126
	ds_read_b32 v128, v142
	ds_read_b32 v142, v144
	ds_read_b32 v143, v143
	ds_read_b32 v127, v127
	ds_read_b32 v145, v129
	ds_read_b32 v144, v181
	ds_read_b32 v129, v180
	s_waitcnt lgkmcnt(4)
	v_pk_add_f32 v[96:97], v[96:97], v[142:143]
	s_waitcnt lgkmcnt(3)
	v_pk_add_f32 v[94:95], v[94:95], v[126:127]
	v_pk_add_f32 v[92:93], v[92:93], v[122:123]
	v_pk_add_f32 v[90:91], v[90:91], v[118:119]
	v_pk_add_f32 v[88:89], v[88:89], v[176:177]
	v_pk_add_f32 v[86:87], v[86:87], v[160:161]
	v_pk_add_f32 v[84:85], v[84:85], v[152:153]
	v_pk_add_f32 v[82:83], v[82:83], v[150:151]
	s_waitcnt lgkmcnt(1)
	v_pk_add_f32 v[80:81], v[80:81], v[144:145]
	s_waitcnt lgkmcnt(0)
	v_pk_add_f32 v[78:79], v[78:79], v[128:129]
	v_pk_add_f32 v[76:77], v[76:77], v[124:125]
	v_pk_add_f32 v[74:75], v[74:75], v[120:121]
	v_pk_add_f32 v[72:73], v[72:73], v[178:179]
	v_pk_add_f32 v[70:71], v[70:71], v[174:175]
	v_pk_add_f32 v[68:69], v[68:69], v[158:159]
	v_pk_add_f32 v[66:67], v[66:67], v[16:17]

.LBB0_2764:
	s_add_i32 s22, s21, -5
	v_add_u32_e32 v3, s0, v233
	ds_read_b64_tr_b16 v[190:191], v3 offset:24576
	ds_read_b64_tr_b16 v[192:193], v3 offset:25088
	v_add_f32_e32 v4, v82, v83
	v_add_f32_e32 v4, v84, v4
	v_add_f32_e32 v4, v85, v4
	v_add_f32_e32 v4, v86, v4
	v_add_f32_e32 v4, v87, v4
	v_cvt_pk_bf16_f32 v114, v82, v83
	v_cvt_pk_bf16_f32 v115, v84, v85
	ds_read_b64_tr_b16 v[186:187], v3 offset:28672
	ds_read_b64_tr_b16 v[188:189], v3 offset:29184
	v_add_f32_e32 v4, v88, v4
	v_add_f32_e32 v4, v89, v4
	v_add_f32_e32 v4, v90, v4
	v_add_f32_e32 v4, v91, v4
	v_cvt_pk_bf16_f32 v116, v86, v87
	v_cvt_pk_bf16_f32 v117, v88, v89
	ds_read_b64_tr_b16 v[182:183], v3 offset:25600
	ds_read_b64_tr_b16 v[184:185], v3 offset:26112
	v_add_f32_e32 v4, v92, v4
	v_add_f32_e32 v4, v93, v4
	v_add_f32_e32 v4, v94, v4
	v_add_f32_e32 v4, v95, v4
	v_cvt_pk_bf16_f32 v118, v90, v91
	v_cvt_pk_bf16_f32 v119, v92, v93
	ds_read_b64_tr_b16 v[178:179], v3 offset:29696
	ds_read_b64_tr_b16 v[180:181], v3 offset:30208
	v_add_f32_e32 v4, v96, v4
	v_add_f32_e32 v4, v97, v4
	v_add_f32_e32 v4, v66, v4
	v_add_f32_e32 v4, v67, v4
	v_cvt_pk_bf16_f32 v120, v94, v95
	v_cvt_pk_bf16_f32 v121, v96, v97
	ds_read_b64_tr_b16 v[174:175], v3 offset:26624
	ds_read_b64_tr_b16 v[176:177], v3 offset:27136
	s_waitcnt lgkmcnt(10)
	v_mfma_f32_32x32x16_bf16 v[82:97], v[130:133], v[110:113], v[50:65]
	v_add_f32_e32 v4, v68, v4
	v_add_f32_e32 v4, v69, v4
	v_add_f32_e32 v4, v70, v4
	v_add_f32_e32 v4, v71, v4
	v_cvt_pk_bf16_f32 v122, v66, v67
	v_cvt_pk_bf16_f32 v123, v68, v69
	ds_read_b64_tr_b16 v[170:171], v3 offset:30720
	ds_read_b64_tr_b16 v[172:173], v3 offset:31232
	v_mfma_f32_32x32x16_bf16 v[82:97], v[142:145], v[106:109], v[82:97]
	v_add_f32_e32 v4, v72, v4
	v_add_f32_e32 v4, v73, v4
	v_add_f32_e32 v4, v74, v4
	v_add_f32_e32 v4, v75, v4
	v_cvt_pk_bf16_f32 v124, v70, v71
	v_cvt_pk_bf16_f32 v125, v72, v73
	ds_read_b64_tr_b16 v[166:167], v3 offset:27648
	ds_read_b64_tr_b16 v[168:169], v3 offset:28160
	v_mfma_f32_32x32x16_bf16 v[82:97], v[150:153], v[102:105], v[82:97]
	v_add_f32_e32 v4, v76, v4
	v_add_f32_e32 v4, v77, v4
	v_add_f32_e32 v4, v78, v4
	v_add_f32_e32 v4, v79, v4
	v_cvt_pk_bf16_f32 v126, v74, v75
	v_cvt_pk_bf16_f32 v127, v76, v77
	ds_read_b64_tr_b16 v[162:163], v3 offset:31744
	ds_read_b64_tr_b16 v[164:165], v3 offset:32256
	v_mfma_f32_32x32x16_bf16 v[82:97], v[158:161], v[98:101], v[82:97]
	v_add_f32_e32 v3, v80, v4
	v_add_f32_e32 v3, v81, v3
	v_add_f32_e32 v3, 0, v3
	v_cvt_pk_bf16_f32 v128, v78, v79
	v_cvt_pk_bf16_f32 v129, v80, v81
	s_waitcnt lgkmcnt(14)
	v_lshl_add_u64 v[4:5], v[200:201], 0, s[54:55]
	s_add_i32 s0, s72, s79
	s_mov_b32 s1, m0
	s_mov_b32 m0, s0
	s_nop 0
	global_load_lds_dwordx4 v[4:5], off
	s_mov_b32 m0, s1
	v_lshl_add_u64 v[4:5], v[198:199], 0, s[54:55]
	s_add_i32 s0, s20, s80
	s_mov_b32 s1, m0
	s_mov_b32 m0, s0
	s_nop 0
	global_load_lds_dwordx4 v[4:5], off
	s_mov_b32 m0, s1
	s_cmp_lt_i32 s22, s78
	v_mfma_f32_32x32x16_bf16 v[66:81], v[134:137], v[110:113], v[50:65]
	v_mfma_f32_32x32x16_bf16 v[66:81], v[138:141], v[106:109], v[66:81]
	v_mfma_f32_32x32x16_bf16 v[66:81], v[146:149], v[102:105], v[66:81]
	v_mfma_f32_32x32x16_bf16 v[66:81], v[154:157], v[98:101], v[66:81]
	s_cbranch_scc1 .LBB0_2766
	ds_read_b128 v[4:7], v235
	ds_read_b128 v[8:11], v235 offset:128
	ds_read_b128 v[12:15], v235 offset:32
	ds_read_b128 v[130:133], v235 offset:160
	s_waitcnt lgkmcnt(3)
	v_sub_u32_e32 v4, v224, v4
	v_sub_u32_e32 v5, v224, v5
	v_sub_u32_e32 v6, v224, v6
	v_sub_u32_e32 v7, v224, v7
	s_waitcnt lgkmcnt(2)
	v_sub_u32_e32 v8, v224, v8
	v_med3_i32 v4, v4, 0, v222
	v_med3_i32 v5, v5, 0, v222
	v_sub_u32_e32 v9, v224, v9
	v_med3_i32 v6, v6, 0, v222
	v_sub_u32_e32 v10, v224, v10
	v_med3_i32 v7, v7, 0, v222
	v_sub_u32_e32 v11, v224, v11
	v_med3_i32 v8, v8, 0, v222
	v_lshl_add_u32 v4, v4, 2, s73
	v_med3_i32 v9, v9, 0, v222
	v_lshl_add_u32 v5, v5, 2, s73
	v_med3_i32 v10, v10, 0, v222
	v_lshl_add_u32 v6, v6, 2, s73
	v_med3_i32 v11, v11, 0, v222
	v_lshl_add_u32 v7, v7, 2, s73
	v_lshl_add_u32 v8, v8, 2, s73
	v_lshl_add_u32 v9, v9, 2, s73
	v_lshl_add_u32 v10, v10, 2, s73
	v_lshl_add_u32 v11, v11, 2, s73
	ds_read_b32 v134, v4
	ds_read_b32 v4, v8
	ds_read_b32 v135, v5
	ds_read_b32 v5, v9
	ds_read_b32 v136, v6
	ds_read_b32 v138, v10
	ds_read_b32 v137, v7
	ds_read_b32 v139, v11
	s_waitcnt lgkmcnt(9)
	v_sub_u32_e32 v6, v224, v12
	s_waitcnt lgkmcnt(8)
	v_sub_u32_e32 v7, v224, v130
	v_med3_i32 v6, v6, 0, v222
	v_med3_i32 v7, v7, 0, v222
	v_lshl_add_u32 v10, v6, 2, s73
	v_lshl_add_u32 v11, v7, 2, s73
	v_sub_u32_e32 v6, v224, v13
	v_sub_u32_e32 v7, v224, v131
	v_med3_i32 v6, v6, 0, v222
	v_med3_i32 v7, v7, 0, v222
	v_lshl_add_u32 v12, v6, 2, s73
	v_lshl_add_u32 v13, v7, 2, s73
	v_sub_u32_e32 v6, v224, v14
	v_sub_u32_e32 v7, v224, v132
	v_med3_i32 v6, v6, 0, v222
	v_med3_i32 v7, v7, 0, v222
	v_lshl_add_u32 v14, v6, 2, s73
	v_lshl_add_u32 v16, v7, 2, s73
	v_sub_u32_e32 v6, v224, v15
	v_sub_u32_e32 v7, v224, v133
	v_med3_i32 v6, v6, 0, v222
	v_med3_i32 v7, v7, 0, v222
	v_lshl_add_u32 v15, v6, 2, s73
	v_lshl_add_u32 v17, v7, 2, s73
	ds_read_b128 v[6:9], v235 offset:64
	ds_read_b32 v140, v10
	ds_read_b32 v142, v11
	ds_read_b32 v141, v12
	ds_read_b32 v143, v13
	ds_read_b32 v144, v14
	ds_read_b32 v146, v16
	ds_read_b32 v145, v15
	ds_read_b32 v147, v17
	ds_read_b128 v[10:13], v235 offset:192
	ds_read_b128 v[14:17], v235 offset:96
	ds_read_b128 v[130:133], v235 offset:224
	s_waitcnt lgkmcnt(11)
	v_sub_u32_e32 v8, v224, v8
	v_med3_i32 v8, v8, 0, v222
	v_sub_u32_e32 v6, v224, v6
	s_waitcnt lgkmcnt(2)
	v_sub_u32_e32 v10, v224, v10
	v_sub_u32_e32 v7, v224, v7
	v_sub_u32_e32 v11, v224, v11
	v_sub_u32_e32 v12, v224, v12
	v_lshl_add_u32 v148, v8, 2, s73
	v_sub_u32_e32 v8, v224, v9
	v_med3_i32 v6, v6, 0, v222
	v_med3_i32 v10, v10, 0, v222
	v_med3_i32 v7, v7, 0, v222
	v_med3_i32 v11, v11, 0, v222
	v_med3_i32 v12, v12, 0, v222
	v_med3_i32 v8, v8, 0, v222
	v_sub_u32_e32 v9, v224, v13
	s_waitcnt lgkmcnt(0)
	v_sub_u32_e32 v131, v224, v131
	v_sub_u32_e32 v16, v224, v16
	v_lshl_add_u32 v6, v6, 2, s73
	v_lshl_add_u32 v10, v10, 2, s73
	v_lshl_add_u32 v7, v7, 2, s73
	v_lshl_add_u32 v11, v11, 2, s73
	v_lshl_add_u32 v12, v12, 2, s73
	v_med3_i32 v9, v9, 0, v222
	v_lshl_add_u32 v13, v8, 2, s73
	v_med3_i32 v131, v131, 0, v222
	v_med3_i32 v16, v16, 0, v222
	v_lshl_add_u32 v149, v9, 2, s73
	ds_read_b32 v6, v6
	ds_read_b32 v8, v10
	ds_read_b32 v7, v7
	ds_read_b32 v9, v11
	ds_read_b32 v10, v148
	ds_read_b32 v12, v12
	ds_read_b32 v11, v13
	ds_read_b32 v13, v149
	v_sub_u32_e32 v14, v224, v14
	v_sub_u32_e32 v130, v224, v130
	v_sub_u32_e32 v15, v224, v15
	v_lshl_add_u32 v148, v131, 2, s73
	v_sub_u32_e32 v131, v224, v132
	v_lshl_add_u32 v132, v16, 2, s73
	v_sub_u32_e32 v16, v224, v17
	v_sub_u32_e32 v17, v224, v133
	v_med3_i32 v14, v14, 0, v222
	v_med3_i32 v130, v130, 0, v222
	v_med3_i32 v15, v15, 0, v222
	v_med3_i32 v131, v131, 0, v222
	v_med3_i32 v16, v16, 0, v222
	v_med3_i32 v17, v17, 0, v222
	v_lshl_add_u32 v14, v14, 2, s73
	v_lshl_add_u32 v130, v130, 2, s73
	v_lshl_add_u32 v15, v15, 2, s73
	v_lshl_add_u32 v149, v131, 2, s73
	v_lshl_add_u32 v131, v16, 2, s73
	v_lshl_add_u32 v17, v17, 2, s73
	ds_read_b32 v14, v14
	ds_read_b32 v16, v130
	ds_read_b32 v130, v132
	ds_read_b32 v131, v131
	ds_read_b32 v15, v15
	ds_read_b32 v133, v17
	ds_read_b32 v132, v149
	ds_read_b32 v17, v148
	s_waitcnt lgkmcnt(4)
	v_pk_add_f32 v[96:97], v[96:97], v[130:131]
	s_waitcnt lgkmcnt(3)
	v_pk_add_f32 v[94:95], v[94:95], v[14:15]
	v_pk_add_f32 v[92:93], v[92:93], v[10:11]
	v_pk_add_f32 v[90:91], v[90:91], v[6:7]
	v_pk_add_f32 v[88:89], v[88:89], v[144:145]
	v_pk_add_f32 v[86:87], v[86:87], v[140:141]
	v_pk_add_f32 v[84:85], v[84:85], v[136:137]
	v_pk_add_f32 v[82:83], v[82:83], v[134:135]
	s_waitcnt lgkmcnt(1)
	v_pk_add_f32 v[80:81], v[80:81], v[132:133]
	s_waitcnt lgkmcnt(0)
	v_pk_add_f32 v[78:79], v[78:79], v[16:17]
	v_pk_add_f32 v[76:77], v[76:77], v[12:13]
	v_pk_add_f32 v[74:75], v[74:75], v[8:9]
	v_pk_add_f32 v[72:73], v[72:73], v[146:147]
	v_pk_add_f32 v[70:71], v[70:71], v[142:143]
	v_pk_add_f32 v[68:69], v[68:69], v[138:139]
	v_pk_add_f32 v[66:67], v[66:67], v[4:5]

.LBB0_2769:
	s_add_i32 s0, s21, -4
	s_add_i32 s1, s20, 0x2000
	v_add_u32_e32 v16, s72, v233
	ds_read_b64_tr_b16 v[134:135], v16 offset:24576
	ds_read_b64_tr_b16 v[136:137], v16 offset:25088
	v_add_f32_e32 v4, v82, v83
	v_add_f32_e32 v4, v84, v4
	v_add_f32_e32 v4, v85, v4
	v_add_f32_e32 v4, v86, v4
	v_add_f32_e32 v4, v87, v4
	v_cvt_pk_bf16_f32 v114, v82, v83
	v_cvt_pk_bf16_f32 v115, v84, v85
	ds_read_b64_tr_b16 v[130:131], v16 offset:28672
	ds_read_b64_tr_b16 v[132:133], v16 offset:29184
	v_add_f32_e32 v4, v88, v4
	v_add_f32_e32 v4, v89, v4
	v_add_f32_e32 v4, v90, v4
	v_add_f32_e32 v4, v91, v4
	v_cvt_pk_bf16_f32 v116, v86, v87
	v_cvt_pk_bf16_f32 v117, v88, v89
	ds_read_b64_tr_b16 v[138:139], v16 offset:25600
	ds_read_b64_tr_b16 v[140:141], v16 offset:26112
	v_add_f32_e32 v4, v92, v4
	v_add_f32_e32 v4, v93, v4
	v_add_f32_e32 v4, v94, v4
	v_add_f32_e32 v4, v95, v4
	v_cvt_pk_bf16_f32 v12, v90, v91
	v_cvt_pk_bf16_f32 v13, v92, v93
	ds_read_b64_tr_b16 v[146:147], v16 offset:29696
	ds_read_b64_tr_b16 v[148:149], v16 offset:30208
	v_add_f32_e32 v4, v96, v4
	v_add_f32_e32 v4, v97, v4
	v_add_f32_e32 v4, v66, v4
	v_add_f32_e32 v4, v67, v4
	v_cvt_pk_bf16_f32 v14, v94, v95
	v_cvt_pk_bf16_f32 v15, v96, v97
	ds_read_b64_tr_b16 v[154:155], v16 offset:26624
	ds_read_b64_tr_b16 v[156:157], v16 offset:27136
	s_waitcnt lgkmcnt(10)
	v_mfma_f32_32x32x16_bf16 v[82:97], v[118:121], v[110:113], v[50:65]
	v_add_f32_e32 v4, v68, v4
	v_add_f32_e32 v4, v69, v4
	v_add_f32_e32 v4, v70, v4
	v_add_f32_e32 v4, v71, v4
	v_cvt_pk_bf16_f32 v8, v66, v67
	v_cvt_pk_bf16_f32 v9, v68, v69
	ds_read_b64_tr_b16 v[170:171], v16 offset:30720
	ds_read_b64_tr_b16 v[172:173], v16 offset:31232
	v_mfma_f32_32x32x16_bf16 v[82:97], v[142:145], v[106:109], v[82:97]
	v_add_f32_e32 v4, v72, v4
	v_add_f32_e32 v4, v73, v4
	v_add_f32_e32 v4, v74, v4
	v_add_f32_e32 v4, v75, v4
	v_cvt_pk_bf16_f32 v10, v70, v71
	v_cvt_pk_bf16_f32 v11, v72, v73
	ds_read_b64_tr_b16 v[166:167], v16 offset:27648
	ds_read_b64_tr_b16 v[168:169], v16 offset:28160
	v_mfma_f32_32x32x16_bf16 v[82:97], v[158:161], v[102:105], v[82:97]
	v_add_f32_e32 v4, v76, v4
	v_add_f32_e32 v4, v77, v4
	v_add_f32_e32 v4, v78, v4
	v_add_f32_e32 v17, v79, v4
	v_cvt_pk_bf16_f32 v4, v74, v75
	v_cvt_pk_bf16_f32 v5, v76, v77
	ds_read_b64_tr_b16 v[162:163], v16 offset:31744
	ds_read_b64_tr_b16 v[164:165], v16 offset:32256
	v_mfma_f32_32x32x16_bf16 v[82:97], v[178:181], v[98:101], v[82:97]
	v_add_f32_e32 v6, v80, v17
	v_add_f32_e32 v6, v81, v6
	v_add_f32_e32 v182, 0, v6
	v_cvt_pk_bf16_f32 v6, v78, v79
	v_cvt_pk_bf16_f32 v7, v80, v81
	s_waitcnt lgkmcnt(14)
	s_cmpk_lg_i32 s20, 0x4000
	s_cselect_b32 s72, s1, 0
	s_add_i32 s1, s20, s79
	s_mov_b32 s8, m0
	s_mov_b32 m0, s1
	s_nop 0
	global_load_lds_dwordx4 v[200:201], off
	s_mov_b32 m0, s8
	s_add_i32 s1, s72, s80
	s_mov_b32 s8, m0
	s_mov_b32 m0, s1
	s_nop 0
	global_load_lds_dwordx4 v[198:199], off
	s_mov_b32 m0, s8
	s_cmp_lt_i32 s0, s78
	v_mfma_f32_32x32x16_bf16 v[66:81], v[122:125], v[110:113], v[50:65]
	v_mfma_f32_32x32x16_bf16 v[66:81], v[126:129], v[106:109], v[66:81]
	v_mfma_f32_32x32x16_bf16 v[66:81], v[150:153], v[102:105], v[66:81]
	v_mfma_f32_32x32x16_bf16 v[66:81], v[174:177], v[98:101], v[66:81]
	s_cbranch_scc1 .LBB0_2771
	ds_read_b128 v[118:121], v235 offset:256
	ds_read_b128 v[122:125], v235 offset:384
	ds_read_b128 v[126:129], v235 offset:288
	ds_read_b128 v[142:145], v235 offset:416
	s_waitcnt lgkmcnt(3)
	v_sub_u32_e32 v16, v224, v118
	s_waitcnt lgkmcnt(2)
	v_sub_u32_e32 v17, v224, v122
	v_sub_u32_e32 v118, v224, v119
	v_sub_u32_e32 v119, v224, v123
	v_med3_i32 v16, v16, 0, v222
	v_med3_i32 v17, v17, 0, v222
	v_med3_i32 v118, v118, 0, v222
	v_med3_i32 v119, v119, 0, v222
	v_sub_u32_e32 v120, v224, v120
	v_sub_u32_e32 v122, v224, v124
	v_sub_u32_e32 v121, v224, v121
	v_sub_u32_e32 v123, v224, v125
	v_lshl_add_u32 v16, v16, 2, s73
	v_lshl_add_u32 v17, v17, 2, s73
	v_lshl_add_u32 v118, v118, 2, s73
	v_lshl_add_u32 v119, v119, 2, s73
	v_med3_i32 v120, v120, 0, v222
	v_med3_i32 v122, v122, 0, v222
	v_med3_i32 v121, v121, 0, v222
	v_med3_i32 v123, v123, 0, v222
	v_lshl_add_u32 v120, v120, 2, s73
	v_lshl_add_u32 v122, v122, 2, s73
	v_lshl_add_u32 v121, v121, 2, s73
	v_lshl_add_u32 v123, v123, 2, s73
	ds_read_b32 v150, v16
	ds_read_b32 v16, v17
	ds_read_b32 v151, v118
	ds_read_b32 v17, v119
	ds_read_b32 v152, v120
	ds_read_b32 v158, v122
	ds_read_b32 v153, v121
	ds_read_b32 v159, v123
	s_waitcnt lgkmcnt(9)
	v_sub_u32_e32 v118, v224, v126
	s_waitcnt lgkmcnt(8)
	v_sub_u32_e32 v119, v224, v142
	v_med3_i32 v118, v118, 0, v222
	v_med3_i32 v119, v119, 0, v222
	v_lshl_add_u32 v122, v118, 2, s73
	v_lshl_add_u32 v123, v119, 2, s73
	v_sub_u32_e32 v118, v224, v127
	v_sub_u32_e32 v119, v224, v143
	v_med3_i32 v118, v118, 0, v222
	v_med3_i32 v119, v119, 0, v222
	v_lshl_add_u32 v124, v118, 2, s73
	v_lshl_add_u32 v125, v119, 2, s73
	v_sub_u32_e32 v118, v224, v128
	v_sub_u32_e32 v119, v224, v144
	v_med3_i32 v118, v118, 0, v222
	v_med3_i32 v119, v119, 0, v222
	v_lshl_add_u32 v126, v118, 2, s73
	v_lshl_add_u32 v127, v119, 2, s73
	v_sub_u32_e32 v118, v224, v129
	v_sub_u32_e32 v119, v224, v145
	v_med3_i32 v118, v118, 0, v222
	v_med3_i32 v119, v119, 0, v222
	v_lshl_add_u32 v128, v118, 2, s73
	v_lshl_add_u32 v129, v119, 2, s73
	ds_read_b128 v[118:121], v235 offset:320
	ds_read_b32 v160, v122
	ds_read_b32 v174, v123
	ds_read_b32 v161, v124
	ds_read_b32 v175, v125
	ds_read_b32 v176, v126
	ds_read_b32 v178, v127
	ds_read_b32 v177, v128
	ds_read_b32 v179, v129
	ds_read_b128 v[122:125], v235 offset:448
	ds_read_b128 v[126:129], v235 offset:352
	ds_read_b128 v[142:145], v235 offset:480
	s_waitcnt lgkmcnt(11)
	v_sub_u32_e32 v120, v224, v120
	v_med3_i32 v120, v120, 0, v222
	v_sub_u32_e32 v118, v224, v118
	s_waitcnt lgkmcnt(2)
	v_sub_u32_e32 v122, v224, v122
	v_sub_u32_e32 v119, v224, v119
	v_sub_u32_e32 v123, v224, v123
	v_sub_u32_e32 v124, v224, v124
	v_lshl_add_u32 v180, v120, 2, s73
	v_sub_u32_e32 v120, v224, v121
	v_med3_i32 v118, v118, 0, v222
	v_med3_i32 v122, v122, 0, v222
	v_med3_i32 v119, v119, 0, v222
	v_med3_i32 v123, v123, 0, v222
	v_med3_i32 v124, v124, 0, v222
	v_med3_i32 v120, v120, 0, v222
	v_sub_u32_e32 v121, v224, v125
	s_waitcnt lgkmcnt(0)
	v_sub_u32_e32 v143, v224, v143
	v_sub_u32_e32 v128, v224, v128
	v_lshl_add_u32 v118, v118, 2, s73
	v_lshl_add_u32 v122, v122, 2, s73
	v_lshl_add_u32 v119, v119, 2, s73
	v_lshl_add_u32 v123, v123, 2, s73
	v_lshl_add_u32 v124, v124, 2, s73
	v_med3_i32 v121, v121, 0, v222
	v_lshl_add_u32 v125, v120, 2, s73
	v_med3_i32 v143, v143, 0, v222
	v_med3_i32 v128, v128, 0, v222
	v_lshl_add_u32 v181, v121, 2, s73
	ds_read_b32 v118, v118
	ds_read_b32 v120, v122
	ds_read_b32 v119, v119
	ds_read_b32 v121, v123
	ds_read_b32 v122, v180
	ds_read_b32 v124, v124
	ds_read_b32 v123, v125
	ds_read_b32 v125, v181
	v_sub_u32_e32 v126, v224, v126
	v_sub_u32_e32 v142, v224, v142
	v_sub_u32_e32 v127, v224, v127
	v_lshl_add_u32 v180, v143, 2, s73
	v_sub_u32_e32 v143, v224, v144
	v_lshl_add_u32 v144, v128, 2, s73
	v_sub_u32_e32 v128, v224, v129
	v_sub_u32_e32 v129, v224, v145
	v_med3_i32 v126, v126, 0, v222
	v_med3_i32 v142, v142, 0, v222
	v_med3_i32 v127, v127, 0, v222
	v_med3_i32 v143, v143, 0, v222
	v_med3_i32 v128, v128, 0, v222
	v_med3_i32 v129, v129, 0, v222
	v_lshl_add_u32 v126, v126, 2, s73
	v_lshl_add_u32 v142, v142, 2, s73
	v_lshl_add_u32 v127, v127, 2, s73
	v_lshl_add_u32 v181, v143, 2, s73
	v_lshl_add_u32 v143, v128, 2, s73
	v_lshl_add_u32 v129, v129, 2, s73
	ds_read_b32 v126, v126
	ds_read_b32 v128, v142
	ds_read_b32 v142, v144
	ds_read_b32 v143, v143
	ds_read_b32 v127, v127
	ds_read_b32 v145, v129
	ds_read_b32 v144, v181
	ds_read_b32 v129, v180
	s_waitcnt lgkmcnt(4)
	v_pk_add_f32 v[96:97], v[96:97], v[142:143]
	s_waitcnt lgkmcnt(3)
	v_pk_add_f32 v[94:95], v[94:95], v[126:127]
	v_pk_add_f32 v[92:93], v[92:93], v[122:123]
	v_pk_add_f32 v[90:91], v[90:91], v[118:119]
	v_pk_add_f32 v[88:89], v[88:89], v[176:177]
	v_pk_add_f32 v[86:87], v[86:87], v[160:161]
	v_pk_add_f32 v[84:85], v[84:85], v[152:153]
	v_pk_add_f32 v[82:83], v[82:83], v[150:151]
	s_waitcnt lgkmcnt(1)
	v_pk_add_f32 v[80:81], v[80:81], v[144:145]
	s_waitcnt lgkmcnt(0)
	v_pk_add_f32 v[78:79], v[78:79], v[128:129]
	v_pk_add_f32 v[76:77], v[76:77], v[124:125]
	v_pk_add_f32 v[74:75], v[74:75], v[120:121]
	v_pk_add_f32 v[72:73], v[72:73], v[178:179]
	v_pk_add_f32 v[70:71], v[70:71], v[174:175]
	v_pk_add_f32 v[68:69], v[68:69], v[158:159]
	v_pk_add_f32 v[66:67], v[66:67], v[16:17]
